# O(1) table lookup of the work unit also in the down-projection loop (replaces the 32-way unrolled schedule walk), reusing the cumulative tile table
# speedup vs baseline: 1.0107x; 1.0032x over previous
; __device__ __forceinline__ bool moe_unit(int cv, int u, int ntiles_n, MoeUnit& mu) {
;     int base = 0;
; #pragma unroll
;     for (int e = 0; e < E; ++e) { const int c = __builtin_amdgcn_readlane(cv, e), tm = (c + 255) >> 8, nu = tm * ntiles_n;
;         if (u < nu) { mu.e = e; mu.cnt = c; mu.base = base; mu.nt = u / tm; mu.mt = u - mu.nt * tm; mu.light = (mu.mt == tm - 1 && c - mu.mt * 256 <= 128) ? 1 : 0; return true; }
;         u -= nu; base += tm * 256; }
;     return false;
; }
; __device__ __forceinline__ void phase_moe_down(const Ptrs& p, LAS unsigned char* lds) {
;     ...
;     for (int u = u0; moe_unit(cv, u, 8, mu); u += G) {
;         if (!all_done) {
;             if (threadIdx.x == 0) {
;                 unsigned* tot = (unsigned*)(p.ws + OFF_GUTOT); unsigned* de = (unsigned*)(p.ws + OFF_GUDONE) + mu.e * 16;
;                 const unsigned need = (unsigned)(((mu.cnt + 255) >> 8) * 16); int all = 0;
.LBB0_1293:
	s_lshr_b32 s2, s62, 3
	v_cmp_ge_i32_e32 vcc, s2, v247
	s_bcnt1_i32_b64 s42, vcc
	v_readlane_b32 s86, v246, 20
	v_readlane_b32 s87, v246, 21
	s_mov_b64 s[0:1], -1
	s_cmp_ge_u32 s42, 32
	s_cbranch_scc1 .LBB0_1292
	s_nop 1
	v_readlane_b32 s83, v1, s42
	v_readlane_b32 s4, v247, s42
	s_add_i32 s3, s83, 0xff
	s_ashr_i32 s3, s3, 8
	s_sub_i32 s4, s4, s3
	s_lshl_b32 s84, s4, 8
	s_lshl_b32 s4, s4, 3
	s_sub_i32 s2, s62, s4
	s_mov_b32 s81, 0
.Lmy_wd_m:
	s_cmp_lt_i32 s2, s3
	s_cbranch_scc1 .Lmy_wd_d
	s_sub_i32 s2, s2, s3
	s_add_i32 s81, s81, 1
	s_branch .Lmy_wd_m
.Lmy_wd_d:
	s_mov_b32 s82, s2
	s_add_i32 s4, s3, -1
	s_cmp_eq_u32 s82, s4
	s_cselect_b64 s[0:1], -1, 0
	s_lshl_b32 s4, s82, 8
	s_sub_i32 s4, s83, s4
	s_cmpk_lt_i32 s4, 0x81
	s_cselect_b64 s[4:5], -1, 0
	s_and_b64 s[0:1], s[0:1], s[4:5]
	v_cndmask_b32_e64 v216, 0, 1, s[0:1]
	s_mov_b64 s[0:1], -1
	s_cmp_lg_u32 s80, 0
	s_cbranch_scc1 .LBB0_1479
	s_mov_b64 s[0:1], exec
	v_readlane_b32 s2, v246, 8
	v_readlane_b32 s3, v246, 9
	s_and_b64 s[2:3], s[0:1], s[2:3]
	s_mov_b64 exec, s[2:3]
	s_cbranch_execz .LBB0_1478
	s_lshl_b32 s2, s42, 4
	s_ashr_i32 s3, s2, 31
	s_lshl_b64 s[2:3], s[2:3], 2
	s_add_u32 s4, s30, s2
	s_addc_u32 s5, s31, s3
	s_add_i32 s2, s83, 0xff
	s_ashr_i32 s2, s2, 4
	s_and_b32 s2, s2, -16
	s_mov_b32 s3, 0x400000
